# last layer: router skips the four all-meta-row tiles (their MoE output is never read), 512 tiles = two rounds
# speedup vs baseline: 1.0359x; 1.0013x over previous
; #define RT_LOADH(tile_) do { const float* hp_ = H + (size_t)((tile_) * 16 + n) * D + wave * 256 + 8 * q; _Pragma("unroll") for (int ks = 0; ks < 8; ++ks) { hv[ks][0] = *(const f32x4*)(hp_ + ks * 32); hv[ks][1] = *(const f32x4*)(hp_ + ks * 32 + 4); } } while (0)
; DI void phase_router(const Args& a, int l, LAS unsigned char* lds, int wave, int lane, int bid, int G, bool dummy = false) {
;     ...
;     const int tid = wave * 64 + lane;
;     const int n = lane & 15, q = lane >> 4;
;     f32x4 hv[8][2];
;     const float* gp = gain + wave * 256 + 8 * q;
;     ...
;     if (bid < T / 16) RT_LOADH(bid);
;     if (wave * 64 + lane < 72) { const int nn_ = wave * 64 + lane; bia[nn_] = (nn_ < 8) ? bco[nn_] : bfi[nn_ - 8]; }
;     for (int tile = bid; tile < T / 16; tile += G) { const int row0 = tile * 16;
.LBB0_1635:
	s_andn2_b64 vcc, exec, s[2:3]
	s_cbranch_vccnz .LBB0_1708
	v_mov_b32_e32 v68, v0
	s_load_dwordx4 s[0:3], s[74:75], 0x108
	v_readfirstlane_b32 s24, v68
	s_mov_b64 s[12:13], s[74:75]
	s_ashr_i32 s7, s24, 6
	v_bfe_u32 v66, v68, 4, 2
	s_waitcnt lgkmcnt(0)
	s_mov_b64 s[26:27], s[2:3]
	s_add_u32 s4, s26, 0x100000
	s_addc_u32 s5, s27, 0
	s_lshl_b32 s28, s7, 8
	s_load_dword s0, s[78:79], 0x0
	s_mov_b32 s1, s72
	s_ashr_i32 s29, s28, 31
	s_waitcnt lgkmcnt(0)
	v_readlane_b32 s32, v255, 30
	s_cmp_eq_u32 s32, 0
	s_cbranch_scc1 .Lrouter_all_tiles
	s_cmpk_lg_i32 s0, 0x100
	s_cbranch_scc1 .Lrouter_all_tiles
	s_lshr_b32 s32, s72, 7
	s_add_i32 s1, s72, s32
	s_add_i32 s1, s1, 1
	s_movk_i32 s0, 0x102
	s_cmpk_gt_u32 s72, 3
	s_cbranch_scc1 .Lrouter_all_tiles
	v_cmp_gt_u32_e32 vcc, 32, v0
	s_and_saveexec_b64 s[82:83], vcc
	s_mul_i32 s32, s72, 0x4080
	s_add_u32 s80, s26, 0x39e31000
	s_addc_u32 s81, s27, 0
	v_lshl_add_u32 v70, v0, 2, s32
	v_add_u32_e32 v71, 0x10200, v70
	v_add_u32_e32 v72, 0x20400, v70
	global_store_dword v70, v91, s[80:81]
	global_store_dword v71, v91, s[80:81]
	global_store_dword v72, v91, s[80:81]
	s_or_b64 exec, exec, s[82:83]
.Lrouter_all_tiles:
	s_cmpk_lt_i32 s1, 0x204
	s_waitcnt vmcnt(9)
	v_and_b32_e32 v97, 15, v68
	s_cselect_b64 s[8:9], -1, 0
	s_cmpk_gt_i32 s1, 0x203
	v_lshlrev_b32_e32 v67, 3, v66
	s_cbranch_scc1 .LBB0_1638
	s_waitcnt vmcnt(7)
	v_lshl_or_b32 v2, s1, 4, v97
	v_ashrrev_i32_e32 v3, 31, v2
	v_lshlrev_b64 v[2:3], 13, v[2:3]
	v_lshl_add_u64 v[2:3], s[4:5], 0, v[2:3]
	v_lshl_add_u64 v[2:3], s[28:29], 2, v[2:3]
	v_lshlrev_b32_e32 v90, 2, v67
	s_waitcnt vmcnt(0)
	v_lshl_add_u64 v[54:55], v[2:3], 0, v[90:91]
	global_load_dwordx4 v[2:5], v[54:55], off offset:16
	global_load_dwordx4 v[6:9], v[54:55], off
	global_load_dwordx4 v[10:13], v[54:55], off offset:144
	global_load_dwordx4 v[14:17], v[54:55], off offset:128
	global_load_dwordx4 v[18:21], v[54:55], off offset:272
	global_load_dwordx4 v[22:25], v[54:55], off offset:256
	global_load_dwordx4 v[26:29], v[54:55], off offset:400
	global_load_dwordx4 v[30:33], v[54:55], off offset:384
	global_load_dwordx4 v[34:37], v[54:55], off offset:528
	global_load_dwordx4 v[38:41], v[54:55], off offset:512
	global_load_dwordx4 v[42:45], v[54:55], off offset:656
	global_load_dwordx4 v[46:49], v[54:55], off offset:640
	global_load_dwordx4 v[62:65], v[54:55], off offset:784
	global_load_dwordx4 v[58:61], v[54:55], off offset:768
	global_load_dwordx4 v[50:53], v[54:55], off offset:912
	s_nop 0
	global_load_dwordx4 v[54:57], v[54:55], off offset:896
